# baseline (speedup 1.0000x reference)
.LBB2_2:
	s_load_dword s3, s[0:1], 0x20
	s_load_dwordx2 s[8:9], s[0:1], 0x10
	s_and_b32 s10, s2, 7
	v_cvt_f32_ubyte0_e32 v3, s10
	v_lshrrev_b32_e32 v12, 4, v0
	s_waitcnt lgkmcnt(0)
	s_mul_hi_i32 s0, s3, 0x2aaaaaab
	s_lshr_b32 s1, s0, 31
	s_ashr_i32 s0, s0, 7
	s_add_i32 s3, s0, s1
	v_cvt_f32_i32_e32 v1, s3
	s_ashr_i32 s0, s3, 30
	s_or_b32 s11, s0, 1
	v_xor_b32_e32 v10, v12, v0
	v_rcp_iflag_f32_e32 v2, v1
	v_lshlrev_b32_e32 v149, 4, v0
	v_mov_b32_e32 v11, 0x60
	v_add_u32_e32 v14, 0, v149
	v_mul_f32_e32 v2, v3, v2
	v_trunc_f32_e32 v2, v2
	v_fma_f32 v3, -v2, v1, v3
	v_cvt_i32_f32_e32 v2, v2
	v_cmp_ge_f32_e64 s[0:1], |v3|, |v1|
	s_and_b64 s[0:1], s[0:1], exec
	s_cselect_b32 s0, s11, 0
	v_readfirstlane_b32 s1, v2
	s_add_i32 s1, s1, s0
	s_bfe_i32 s0, s1, 0x170000
	s_mul_i32 s0, s0, s3
	s_sub_i32 s0, s10, s0
	s_lshl_b32 s0, s0, 2
	s_lshr_b32 s3, s2, 6
	s_add_i32 s13, s0, s3
	s_lshl_b32 s0, s2, 5
	s_lshl_b32 s15, s1, 11
	s_and_b32 s18, s0, 0x700
	s_or_b32 s12, s15, s18
	v_lshrrev_b32_e32 v1, 3, v0
	v_or_b32_e32 v2, s12, v1
	s_mulk_i32 s13, 0xc0
	v_ashrrev_i32_e32 v3, 31, v2
	v_lshlrev_b64 v[4:5], 11, v[2:3]
	v_or_b32_e32 v2, s13, v1
	v_mov_b32_e32 v3, 0
	v_lshlrev_b64 v[6:7], 11, v[2:3]
	v_lshlrev_b32_e32 v2, 4, v10
	v_and_b32_e32 v10, 64, v0
	v_cmp_ne_u32_e32 vcc, 0, v10
	v_and_b32_e32 v143, 15, v0
	v_lshl_add_u64 v[4:5], s[4:5], 0, v[4:5]
	v_and_b32_e32 v2, 0x70, v2
	v_cndmask_b32_e32 v142, 0, v11, vcc
	v_readfirstlane_b32 s0, v14
	v_add_u32_e32 v16, 0x2000, v14
	v_lshl_add_u64 v[4:5], v[4:5], 0, v[2:3]
	v_or_b32_e32 v10, v142, v143
	s_mov_b32 m0, s0
	s_mov_b64 s[0:1], 0x20000
	v_readfirstlane_b32 s2, v16
	v_add_u32_e32 v16, 0x4000, v14
	v_lshlrev_b32_e32 v146, 7, v10
	global_load_lds_dwordx4 v[4:5], off
	v_lshl_add_u64 v[10:11], v[4:5], 0, s[0:1]
	s_mov_b32 m0, s2
	s_mov_b64 s[2:3], 0x40000
	v_readfirstlane_b32 s10, v16
	global_load_lds_dwordx4 v[10:11], off
	v_lshl_add_u64 v[10:11], v[4:5], 0, s[2:3]
	s_mov_b32 m0, s10
	s_mov_b64 s[10:11], 0x60000
	v_add_u32_e32 v16, 0x6000, v14
	v_lshl_add_u64 v[8:9], s[6:7], 0, v[6:7]
	v_add_u32_e32 v15, 0x8000, v14
	global_load_lds_dwordx4 v[10:11], off
	v_lshl_add_u64 v[10:11], v[4:5], 0, s[10:11]
	v_readfirstlane_b32 s10, v16
	v_lshl_add_u64 v[8:9], v[8:9], 0, v[2:3]
	v_and_b32_e32 v209, 7, v0
	v_lshlrev_b32_e32 v209, 5, v209
	ds_bpermute_b32 v210, v209, v4
	ds_bpermute_b32 v211, v209, v5
	ds_bpermute_b32 v212, v209, v8
	ds_bpermute_b32 v213, v209, v9
	v_bfe_u32 v214, v0, 3, 3
	v_min_u32_e32 v214, 6, v214
	v_cmp_gt_u32_e64 s[24:25], 4, v214
	v_and_b32_e32 v214, 3, v214
	v_lshlrev_b32_e32 v214, 17, v214
	v_mov_b32_e32 v215, 0
	s_waitcnt lgkmcnt(0)
	v_cndmask_b32_e64 v210, v212, v210, s[24:25]
	v_cndmask_b32_e64 v211, v213, v211, s[24:25]
	v_lshl_add_u64 v[210:211], v[210:211], 0, v[214:215]
	global_load_dword v208, v[210:211], off offset:256
	global_load_dword v208, v[210:211], off offset:384
	global_load_dword v208, v[210:211], off offset:512
	s_mov_b32 m0, s10
	v_readfirstlane_b32 s10, v15
	v_add_u32_e32 v15, 0xa000, v14
	v_lshrrev_b32_e32 v2, 1, v0
	global_load_lds_dwordx4 v[10:11], off
	s_mov_b32 m0, s10
	v_lshl_add_u64 v[10:11], v[8:9], 0, s[0:1]
	v_readfirstlane_b32 s0, v15
	v_add_u32_e32 v15, 0xc000, v14
	v_bfe_u32 v145, v0, 4, 2
	v_and_b32_e32 v141, 0xc0, v2
	global_load_lds_dwordx4 v[8:9], off
	s_mov_b32 m0, s0
	v_readfirstlane_b32 s0, v15
	v_bitop3_b32 v13, v145, v2, 7 bitop3:0x78
	v_or_b32_e32 v2, v141, v143
	global_load_lds_dwordx4 v[10:11], off
	s_mov_b32 m0, s0
	s_add_i32 s0, 0, 0x16000
	v_add_u32_e32 v15, 0xe000, v14
	v_lshl_add_u64 v[10:11], v[8:9], 0, s[2:3]
	v_lshlrev_b32_e32 v147, 7, v2
	v_add_u32_e32 v2, s0, v149
	s_mov_b64 s[0:1], 0x80
	v_readfirstlane_b32 s2, v15
	v_add_u32_e32 v15, 0x10000, v14
	global_load_lds_dwordx4 v[10:11], off
	v_lshl_add_u64 v[10:11], v[4:5], 0, s[0:1]
	s_mov_b32 m0, s2
	s_mov_b64 s[2:3], 0x20080
	v_readfirstlane_b32 s10, v15
	v_add_u32_e32 v15, 0x12000, v14
	global_load_lds_dwordx4 v[10:11], off
	v_lshl_add_u64 v[10:11], v[4:5], 0, s[2:3]
	s_mov_b32 m0, s10
	s_mov_b64 s[10:11], 0x40080
	v_readfirstlane_b32 s16, v15
	global_load_lds_dwordx4 v[10:11], off
	v_lshl_add_u64 v[10:11], v[4:5], 0, s[10:11]
	s_mov_b32 m0, s16
	s_mov_b64 s[16:17], 0x60080
	global_load_lds_dwordx4 v[10:11], off
	v_add_u32_e32 v10, 0x14000, v14
	v_lshl_add_u64 v[4:5], v[4:5], 0, s[16:17]
	v_readfirstlane_b32 s16, v10
	s_mov_b32 m0, s16
	v_add_u32_e32 v10, 0x2000, v2
	global_load_lds_dwordx4 v[4:5], off
	v_lshl_add_u64 v[4:5], v[8:9], 0, s[0:1]
	v_readfirstlane_b32 s0, v2
	s_mov_b32 m0, s0
	v_readfirstlane_b32 s0, v10
	v_add_u32_e32 v2, 0x4000, v2
	global_load_lds_dwordx4 v[4:5], off
	v_lshl_add_u64 v[4:5], v[8:9], 0, s[2:3]
	s_mov_b32 m0, s0
	v_readfirstlane_b32 s0, v2
	global_load_lds_dwordx4 v[4:5], off
	v_lshl_add_u64 v[4:5], v[8:9], 0, s[10:11]
	s_mov_b32 m0, s0
	v_lshlrev_b32_e32 v2, 4, v13
	global_load_lds_dwordx4 v[4:5], off
	s_waitcnt vmcnt(7) lgkmcnt(0)
	s_barrier
	v_add3_u32 v150, 0, v147, v2
	v_add3_u32 v151, 0, v146, v2
	ds_read_b128 v[118:121], v150
	ds_read_b128 v[106:109], v150 offset:2048
	ds_read_b128 v[86:89], v150 offset:4096
	ds_read_b128 v[34:37], v150 offset:6144
	ds_read_b128 v[98:101], v151 offset:32768
	ds_read_b128 v[90:93], v151 offset:34816
	ds_read_b128 v[82:85], v151 offset:36864
	ds_read_b128 v[74:77], v151 offset:38912
	ds_read_b128 v[66:69], v151 offset:40960
	ds_read_b128 v[50:53], v151 offset:43008
	v_or_b32_e32 v1, s15, v1
	v_or_b32_e32 v4, s18, v1
	v_and_b32_e32 v140, 63, v0
	v_lshrrev_b32_e32 v144, 6, v0
	v_ashrrev_i32_e32 v5, 31, v4
	v_bitop3_b32 v0, v12, 7, v0 bitop3:0x48
	v_xor_b32_e32 v148, 64, v2
	v_lshlrev_b64 v[4:5], 11, v[4:5]
	v_lshlrev_b32_e32 v2, 4, v0
	v_or_b32_e32 v4, v4, v2
	v_or_b32_e32 v6, v6, v2
	s_mov_b32 s14, 0
	v_lshl_add_u64 v[0:1], s[4:5], 0, v[4:5]
	v_lshl_add_u64 v[138:139], s[6:7], 0, v[6:7]
	s_mov_b64 s[0:1], 0
	s_mov_b64 s[2:3], 0x100
	s_mov_b64 s[4:5], 0x20100
	s_mov_b64 s[6:7], 0x40100
	s_mov_b64 s[10:11], 0x60100
	v_lshl_add_u64 v[192:193], v[0:1], 0, s[2:3]
	v_lshl_add_u64 v[194:195], v[0:1], 0, s[4:5]
	v_lshl_add_u64 v[196:197], v[0:1], 0, s[6:7]
	v_lshl_add_u64 v[198:199], v[0:1], 0, s[10:11]
	v_lshl_add_u64 v[200:201], v[138:139], 0, s[2:3]
	v_lshl_add_u64 v[202:203], v[138:139], 0, s[4:5]
	v_lshl_add_u64 v[204:205], v[138:139], 0, s[6:7]
	v_readfirstlane_b32 s21, v149
	s_mov_b64 s[22:23], 0x80
	v_mov_b32_e32 v2, v3
	v_mov_b32_e32 v4, v3
	v_mov_b32_e32 v5, v3
	v_mov_b32_e32 v6, v3
	v_mov_b32_e32 v7, v3
	v_mov_b32_e32 v8, v3
	v_mov_b32_e32 v9, v3
	v_mov_b32_e32 v10, v3
	v_mov_b32_e32 v11, v3
	v_mov_b32_e32 v12, v3
	v_mov_b32_e32 v13, v3
	v_mov_b32_e32 v14, v3
	v_mov_b32_e32 v15, v3
	v_mov_b32_e32 v16, v3
	v_mov_b32_e32 v17, v3
	v_mov_b32_e32 v18, v3
	v_mov_b32_e32 v19, v3
	v_mov_b32_e32 v20, v3
	v_mov_b32_e32 v21, v3
	v_mov_b32_e32 v22, v3
	v_mov_b32_e32 v23, v3
	v_mov_b32_e32 v24, v3
	v_mov_b32_e32 v25, v3
	v_mov_b32_e32 v26, v3
	v_mov_b32_e32 v27, v3
	v_mov_b32_e32 v28, v3
	v_mov_b32_e32 v29, v3
	v_mov_b32_e32 v30, v3
	v_mov_b32_e32 v31, v3
	v_mov_b32_e32 v32, v3
	v_mov_b32_e32 v33, v3
	v_mov_b32_e32 v38, v3
	v_mov_b32_e32 v39, v3
	v_mov_b32_e32 v40, v3
	v_mov_b32_e32 v41, v3
	v_mov_b32_e32 v42, v3
	v_mov_b32_e32 v43, v3
	v_mov_b32_e32 v44, v3
	v_mov_b32_e32 v45, v3
	v_mov_b32_e32 v46, v3
	v_mov_b32_e32 v47, v3
	v_mov_b32_e32 v48, v3
	v_mov_b32_e32 v49, v3
	v_mov_b32_e32 v54, v3
	v_mov_b32_e32 v55, v3
	v_mov_b32_e32 v56, v3
	v_mov_b32_e32 v57, v3
	v_mov_b32_e32 v58, v3
	v_mov_b32_e32 v59, v3
	v_mov_b32_e32 v60, v3
	v_mov_b32_e32 v61, v3
	v_mov_b32_e32 v62, v3
	v_mov_b32_e32 v63, v3
	v_mov_b32_e32 v64, v3
	v_mov_b32_e32 v65, v3
	v_mov_b32_e32 v70, v3
	v_mov_b32_e32 v71, v3
	v_mov_b32_e32 v72, v3
	v_mov_b32_e32 v73, v3
	v_mov_b32_e32 v78, v3
	v_mov_b32_e32 v79, v3
	v_mov_b32_e32 v80, v3
	v_mov_b32_e32 v81, v3
	v_mov_b32_e32 v94, v3
	v_mov_b32_e32 v95, v3
	v_mov_b32_e32 v96, v3
	v_mov_b32_e32 v97, v3
	v_mov_b32_e32 v102, v3
	v_mov_b32_e32 v103, v3
	v_mov_b32_e32 v104, v3
	v_mov_b32_e32 v105, v3
	v_mov_b32_e32 v110, v3
	v_mov_b32_e32 v111, v3
	v_mov_b32_e32 v112, v3
	v_mov_b32_e32 v113, v3
	v_mov_b32_e32 v114, v3
	v_mov_b32_e32 v115, v3
	v_mov_b32_e32 v116, v3
	v_mov_b32_e32 v117, v3
	v_mov_b32_e32 v122, v3
	v_mov_b32_e32 v123, v3
	v_mov_b32_e32 v124, v3
	v_mov_b32_e32 v125, v3
	v_mov_b32_e32 v126, v3
	v_mov_b32_e32 v127, v3
	v_mov_b32_e32 v128, v3
	v_mov_b32_e32 v129, v3
	v_mov_b32_e32 v130, v3
	v_mov_b32_e32 v131, v3
	v_mov_b32_e32 v132, v3
	v_mov_b32_e32 v133, v3
	v_mov_b32_e32 v134, v3
	v_mov_b32_e32 v135, v3
	v_mov_b32_e32 v136, v3
	v_mov_b32_e32 v137, v3
.LBB2_3:
	s_mul_i32 s15, s14, 0xe000
	s_add_i32 s14, s14, 1
	s_cmp_lg_u32 s14, 2
	s_cselect_b32 s14, s14, 0
	s_add_i32 s20, s15, s21
	v_add3_u32 v206, s15, v147, v148
	v_add3_u32 v207, s15, v146, v148
	s_waitcnt lgkmcnt(8)
	v_mfma_f32_16x16x32_f16 v[134:137], v[98:101], v[118:121], v[134:137]
	s_waitcnt lgkmcnt(7)
	v_mfma_f32_16x16x32_f16 v[130:133], v[90:93], v[118:121], v[130:133]
	s_waitcnt lgkmcnt(6)
	v_mfma_f32_16x16x32_f16 v[102:105], v[98:101], v[106:109], v[102:105]
	ds_read_b128 v[152:155], v206
	v_mfma_f32_16x16x32_f16 v[94:97], v[90:93], v[106:109], v[94:97]
	ds_read_b128 v[168:171], v207 offset:32768
	s_waitcnt lgkmcnt(7)
	v_mfma_f32_16x16x32_f16 v[126:129], v[82:85], v[118:121], v[126:129]
	ds_read_b128 v[172:175], v207 offset:34816
	v_mfma_f32_16x16x32_f16 v[78:81], v[82:85], v[106:109], v[78:81]
	ds_read_b128 v[156:159], v206 offset:2048
	s_waitcnt lgkmcnt(8)
	v_mfma_f32_16x16x32_f16 v[122:125], v[74:77], v[118:121], v[122:125]
	ds_read_b128 v[176:179], v207 offset:36864
	v_mfma_f32_16x16x32_f16 v[70:73], v[74:77], v[106:109], v[70:73]
	ds_read_b128 v[180:183], v207 offset:38912
	s_waitcnt lgkmcnt(9)
	v_mfma_f32_16x16x32_f16 v[54:57], v[98:101], v[86:89], v[54:57]
	ds_read_b128 v[160:163], v206 offset:4096
	v_mfma_f32_16x16x32_f16 v[46:49], v[90:93], v[86:89], v[46:49]
	ds_read_b128 v[184:187], v207 offset:40960
	v_mfma_f32_16x16x32_f16 v[42:45], v[82:85], v[86:89], v[42:45]
	ds_read_b128 v[188:191], v207 offset:43008
	v_mfma_f32_16x16x32_f16 v[38:41], v[74:77], v[86:89], v[38:41]
	ds_read_b128 v[164:167], v206 offset:6144
	s_waitcnt lgkmcnt(12)
	v_mfma_f32_16x16x32_f16 v[114:117], v[66:69], v[118:121], v[114:117]
	v_mfma_f32_16x16x32_f16 v[62:65], v[66:69], v[106:109], v[62:65]
	v_mfma_f32_16x16x32_f16 v[30:33], v[66:69], v[86:89], v[30:33]
	s_waitcnt lgkmcnt(11)
	v_mfma_f32_16x16x32_f16 v[110:113], v[50:53], v[118:121], v[110:113]
	v_mfma_f32_16x16x32_f16 v[58:61], v[50:53], v[106:109], v[58:61]
	v_mfma_f32_16x16x32_f16 v[26:29], v[50:53], v[86:89], v[26:29]
	s_waitcnt lgkmcnt(10)
	v_mfma_f32_16x16x32_f16 v[22:25], v[98:101], v[34:37], v[22:25]
	v_mfma_f32_16x16x32_f16 v[18:21], v[90:93], v[34:37], v[18:21]
	v_mfma_f32_16x16x32_f16 v[14:17], v[82:85], v[34:37], v[14:17]
	v_mfma_f32_16x16x32_f16 v[10:13], v[74:77], v[34:37], v[10:13]
	v_mfma_f32_16x16x32_f16 v[6:9], v[66:69], v[34:37], v[6:9]
	v_mfma_f32_16x16x32_f16 v[2:5], v[50:53], v[34:37], v[2:5]
	s_waitcnt vmcnt(0) lgkmcnt(0)
	s_barrier
	s_mov_b32 m0, s20
	s_mul_i32 s15, s14, 0xe000
	v_mfma_f32_16x16x32_f16 v[134:137], v[168:171], v[152:155], v[134:137]
	global_load_lds_dwordx4 v[192:193], off
	v_lshl_add_u64 v[192:193], v[192:193], 0, s[22:23]
	s_add_u32 m0, s20, 0x2000
	v_mfma_f32_16x16x32_f16 v[130:133], v[172:175], v[152:155], v[130:133]
	v_mfma_f32_16x16x32_f16 v[126:129], v[176:179], v[152:155], v[126:129]
	global_load_lds_dwordx4 v[194:195], off
	v_lshl_add_u64 v[194:195], v[194:195], 0, s[22:23]
	s_add_u32 m0, s20, 0x4000
	v_mfma_f32_16x16x32_f16 v[122:125], v[180:183], v[152:155], v[122:125]
	v_mfma_f32_16x16x32_f16 v[114:117], v[184:187], v[152:155], v[114:117]
	global_load_lds_dwordx4 v[196:197], off
	v_lshl_add_u64 v[196:197], v[196:197], 0, s[22:23]
	s_add_u32 m0, s20, 0x6000
	v_mfma_f32_16x16x32_f16 v[110:113], v[188:191], v[152:155], v[110:113]
	v_mfma_f32_16x16x32_f16 v[102:105], v[168:171], v[156:159], v[102:105]
	global_load_lds_dwordx4 v[198:199], off
	v_lshl_add_u64 v[198:199], v[198:199], 0, s[22:23]
	s_add_u32 m0, s20, 0x8000
	v_mfma_f32_16x16x32_f16 v[94:97], v[172:175], v[156:159], v[94:97]
	v_mfma_f32_16x16x32_f16 v[78:81], v[176:179], v[156:159], v[78:81]
	global_load_lds_dwordx4 v[200:201], off
	v_lshl_add_u64 v[200:201], v[200:201], 0, s[22:23]
	s_add_u32 m0, s20, 0xa000
	v_mfma_f32_16x16x32_f16 v[70:73], v[180:183], v[156:159], v[70:73]
	v_mfma_f32_16x16x32_f16 v[62:65], v[184:187], v[156:159], v[62:65]
	global_load_lds_dwordx4 v[202:203], off
	v_lshl_add_u64 v[202:203], v[202:203], 0, s[22:23]
	s_add_u32 m0, s20, 0xc000
	v_mfma_f32_16x16x32_f16 v[58:61], v[188:191], v[156:159], v[58:61]
	v_mfma_f32_16x16x32_f16 v[54:57], v[168:171], v[160:163], v[54:57]
	global_load_lds_dwordx4 v[204:205], off
	v_lshl_add_u64 v[204:205], v[204:205], 0, s[22:23]
	v_add_u32_e32 v206, s15, v150
	v_add_u32_e32 v207, s15, v151
	v_mfma_f32_16x16x32_f16 v[46:49], v[172:175], v[160:163], v[46:49]
	v_mfma_f32_16x16x32_f16 v[42:45], v[176:179], v[160:163], v[42:45]
	ds_read_b128 v[118:121], v206
	v_mfma_f32_16x16x32_f16 v[38:41], v[180:183], v[160:163], v[38:41]
	ds_read_b128 v[98:101], v207 offset:32768
	v_mfma_f32_16x16x32_f16 v[30:33], v[184:187], v[160:163], v[30:33]
	ds_read_b128 v[90:93], v207 offset:34816
	v_mfma_f32_16x16x32_f16 v[26:29], v[188:191], v[160:163], v[26:29]
	ds_read_b128 v[106:109], v206 offset:2048
	v_mfma_f32_16x16x32_f16 v[22:25], v[168:171], v[164:167], v[22:25]
	ds_read_b128 v[82:85], v207 offset:36864
	v_mfma_f32_16x16x32_f16 v[18:21], v[172:175], v[164:167], v[18:21]
	ds_read_b128 v[74:77], v207 offset:38912
	v_mfma_f32_16x16x32_f16 v[14:17], v[176:179], v[164:167], v[14:17]
	ds_read_b128 v[86:89], v206 offset:4096
	v_mfma_f32_16x16x32_f16 v[10:13], v[180:183], v[164:167], v[10:13]
	ds_read_b128 v[66:69], v207 offset:40960
	v_mfma_f32_16x16x32_f16 v[6:9], v[184:187], v[164:167], v[6:9]
	ds_read_b128 v[50:53], v207 offset:43008
	v_mfma_f32_16x16x32_f16 v[2:5], v[188:191], v[164:167], v[2:5]
	ds_read_b128 v[34:37], v206 offset:6144
	s_add_u32 s0, s0, 0x80
	s_addc_u32 s1, s1, 0
	s_cmpk_eq_i32 s0, 0x700
	s_cbranch_scc0 .LBB2_3
	s_add_i32 s0, s15, 0
	v_add3_u32 v0, s0, v147, v148
	s_waitcnt lgkmcnt(0)
	v_mfma_f32_16x16x32_f16 v[134:137], v[98:101], v[118:121], v[134:137]
	s_add_i32 s1, s14, 1
	s_cmp_lg_u32 s1, 2
	s_cselect_b32 s1, s1, 0
	v_mfma_f32_16x16x32_f16 v[130:133], v[90:93], v[118:121], v[130:133]
	v_mfma_f32_16x16x32_f16 v[126:129], v[82:85], v[118:121], v[126:129]
	v_mfma_f32_16x16x32_f16 v[102:105], v[98:101], v[106:109], v[102:105]
	v_mfma_f32_16x16x32_f16 v[94:97], v[90:93], v[106:109], v[94:97]
	v_mfma_f32_16x16x32_f16 v[78:81], v[82:85], v[106:109], v[78:81]
	v_mfma_f32_16x16x32_f16 v[54:57], v[98:101], v[86:89], v[54:57]
	v_mfma_f32_16x16x32_f16 v[46:49], v[90:93], v[86:89], v[46:49]
	v_mfma_f32_16x16x32_f16 v[42:45], v[82:85], v[86:89], v[42:45]
	v_mfma_f32_16x16x32_f16 v[38:41], v[74:77], v[86:89], v[38:41]
	v_mfma_f32_16x16x32_f16 v[30:33], v[66:69], v[86:89], v[30:33]
	v_mfma_f32_16x16x32_f16 v[26:29], v[50:53], v[86:89], v[26:29]
	v_mfma_f32_16x16x32_f16 v[22:25], v[98:101], v[34:37], v[22:25]
	v_mfma_f32_16x16x32_f16 v[18:21], v[90:93], v[34:37], v[18:21]
	ds_read_b128 v[86:89], v0
	ds_read_b128 v[90:93], v0 offset:2048
	v_mfma_f32_16x16x32_f16 v[14:17], v[82:85], v[34:37], v[14:17]
	ds_read_b128 v[82:85], v0 offset:4096
	ds_read_b128 v[98:101], v0 offset:6144
	v_add3_u32 v0, s0, v146, v148
	v_mfma_f32_16x16x32_f16 v[122:125], v[74:77], v[118:121], v[122:125]
	v_mfma_f32_16x16x32_f16 v[114:117], v[66:69], v[118:121], v[114:117]
	v_mfma_f32_16x16x32_f16 v[110:113], v[50:53], v[118:121], v[110:113]
	v_mfma_f32_16x16x32_f16 v[70:73], v[74:77], v[106:109], v[70:73]
	v_mfma_f32_16x16x32_f16 v[62:65], v[66:69], v[106:109], v[62:65]
	v_mfma_f32_16x16x32_f16 v[58:61], v[50:53], v[106:109], v[58:61]
	v_mfma_f32_16x16x32_f16 v[10:13], v[74:77], v[34:37], v[10:13]
	ds_read_b128 v[74:77], v0 offset:32768
	ds_read_b128 v[106:109], v0 offset:34816
	v_mfma_f32_16x16x32_f16 v[6:9], v[66:69], v[34:37], v[6:9]
	ds_read_b128 v[66:69], v0 offset:36864
	ds_read_b128 v[118:121], v0 offset:38912
	ds_read_b128 v[152:155], v0 offset:40960
	ds_read_b128 v[156:159], v0 offset:43008
	v_mfma_f32_16x16x32_f16 v[0:3], v[50:53], v[34:37], v[2:5]
	s_mul_i32 s1, s1, 0xe000
	s_waitcnt vmcnt(0) lgkmcnt(0)
	s_barrier
	v_add_u32_e32 v4, s1, v150
	ds_read_b128 v[34:37], v4
	ds_read_b128 v[50:53], v4 offset:2048
	ds_read_b128 v[160:163], v4 offset:4096
	ds_read_b128 v[164:167], v4 offset:6144
	v_add_u32_e32 v4, s1, v151
	ds_read_b128 v[168:171], v4 offset:32768
	ds_read_b128 v[172:175], v4 offset:34816
	ds_read_b128 v[176:179], v4 offset:36864
	ds_read_b128 v[180:183], v4 offset:38912
	ds_read_b128 v[184:187], v4 offset:40960
	ds_read_b128 v[188:191], v4 offset:43008
	v_mfma_f32_16x16x32_f16 v[134:137], v[74:77], v[86:89], v[134:137]
	v_mfma_f32_16x16x32_f16 v[130:133], v[106:109], v[86:89], v[130:133]
	v_mfma_f32_16x16x32_f16 v[126:129], v[66:69], v[86:89], v[126:129]
	v_mfma_f32_16x16x32_f16 v[122:125], v[118:121], v[86:89], v[122:125]
	v_mfma_f32_16x16x32_f16 v[114:117], v[152:155], v[86:89], v[114:117]
	v_mfma_f32_16x16x32_f16 v[86:89], v[156:159], v[86:89], v[110:113]
	v_mfma_f32_16x16x32_f16 v[102:105], v[74:77], v[90:93], v[102:105]
	v_mfma_f32_16x16x32_f16 v[94:97], v[106:109], v[90:93], v[94:97]
	v_mfma_f32_16x16x32_f16 v[78:81], v[66:69], v[90:93], v[78:81]
	v_mfma_f32_16x16x32_f16 v[70:73], v[118:121], v[90:93], v[70:73]
	v_mfma_f32_16x16x32_f16 v[62:65], v[152:155], v[90:93], v[62:65]
	v_mfma_f32_16x16x32_f16 v[58:61], v[156:159], v[90:93], v[58:61]
	v_mfma_f32_16x16x32_f16 v[54:57], v[74:77], v[82:85], v[54:57]
	v_mfma_f32_16x16x32_f16 v[46:49], v[106:109], v[82:85], v[46:49]
	v_mfma_f32_16x16x32_f16 v[42:45], v[66:69], v[82:85], v[42:45]
	v_mfma_f32_16x16x32_f16 v[38:41], v[118:121], v[82:85], v[38:41]
	v_mfma_f32_16x16x32_f16 v[30:33], v[152:155], v[82:85], v[30:33]
	v_mfma_f32_16x16x32_f16 v[26:29], v[156:159], v[82:85], v[26:29]
	v_mfma_f32_16x16x32_f16 v[22:25], v[74:77], v[98:101], v[22:25]
	v_mfma_f32_16x16x32_f16 v[18:21], v[106:109], v[98:101], v[18:21]
	v_mfma_f32_16x16x32_f16 v[14:17], v[66:69], v[98:101], v[14:17]
	v_mfma_f32_16x16x32_f16 v[10:13], v[118:121], v[98:101], v[10:13]
	v_mfma_f32_16x16x32_f16 v[4:7], v[152:155], v[98:101], v[6:9]
	v_mfma_f32_16x16x32_f16 v[0:3], v[156:159], v[98:101], v[0:3]
	s_add_i32 s0, s1, 0
	s_nop 0
	v_add3_u32 v8, s0, v147, v148
	s_waitcnt lgkmcnt(5)
	v_mfma_f32_16x16x32_f16 v[66:69], v[168:171], v[34:37], v[134:137]
	s_waitcnt lgkmcnt(4)
	v_mfma_f32_16x16x32_f16 v[74:77], v[172:175], v[34:37], v[130:133]
	s_waitcnt lgkmcnt(3)
	v_mfma_f32_16x16x32_f16 v[82:85], v[176:179], v[34:37], v[126:129]
	s_waitcnt lgkmcnt(2)
	v_mfma_f32_16x16x32_f16 v[90:93], v[180:183], v[34:37], v[122:125]
	s_waitcnt lgkmcnt(1)
	v_mfma_f32_16x16x32_f16 v[98:101], v[184:187], v[34:37], v[114:117]
	s_waitcnt lgkmcnt(0)
	v_mfma_f32_16x16x32_f16 v[34:37], v[188:191], v[34:37], v[86:89]
	v_mfma_f32_16x16x32_f16 v[86:89], v[168:171], v[50:53], v[102:105]
	v_mfma_f32_16x16x32_f16 v[94:97], v[172:175], v[50:53], v[94:97]
	v_mfma_f32_16x16x32_f16 v[78:81], v[176:179], v[50:53], v[78:81]
	v_mfma_f32_16x16x32_f16 v[70:73], v[180:183], v[50:53], v[70:73]
	v_mfma_f32_16x16x32_f16 v[62:65], v[184:187], v[50:53], v[62:65]
	v_mfma_f32_16x16x32_f16 v[50:53], v[188:191], v[50:53], v[58:61]
	s_nop 2
	ds_read_b128 v[58:61], v8
	ds_read_b128 v[102:105], v8 offset:2048
	ds_read_b128 v[106:109], v8 offset:4096
	ds_read_b128 v[110:113], v8 offset:6144
	v_mfma_f32_16x16x32_f16 v[8:11], v[180:183], v[164:167], v[10:13]
	s_nop 2
	v_add3_u32 v12, s0, v146, v148
	ds_read_b128 v[114:117], v12 offset:32768
	ds_read_b128 v[118:121], v12 offset:34816
	ds_read_b128 v[122:125], v12 offset:36864
	ds_read_b128 v[126:129], v12 offset:38912
	ds_read_b128 v[130:133], v12 offset:40960
	ds_read_b128 v[134:137], v12 offset:43008
	v_mfma_f32_16x16x32_f16 v[54:57], v[168:171], v[160:163], v[54:57]
	v_mfma_f32_16x16x32_f16 v[46:49], v[172:175], v[160:163], v[46:49]
	v_mfma_f32_16x16x32_f16 v[42:45], v[176:179], v[160:163], v[42:45]
	v_mfma_f32_16x16x32_f16 v[38:41], v[180:183], v[160:163], v[38:41]
	v_mfma_f32_16x16x32_f16 v[30:33], v[184:187], v[160:163], v[30:33]
	v_mfma_f32_16x16x32_f16 v[26:29], v[188:191], v[160:163], v[26:29]
	v_mfma_f32_16x16x32_f16 v[22:25], v[168:171], v[164:167], v[22:25]
	v_mfma_f32_16x16x32_f16 v[18:21], v[172:175], v[164:167], v[18:21]
	v_mfma_f32_16x16x32_f16 v[14:17], v[176:179], v[164:167], v[14:17]
	v_mfma_f32_16x16x32_f16 v[4:7], v[184:187], v[164:167], v[4:7]
	v_mfma_f32_16x16x32_f16 v[0:3], v[188:191], v[164:167], v[0:3]
	s_waitcnt vmcnt(0) lgkmcnt(0)
	s_barrier
	v_mfma_f32_16x16x32_f16 v[66:69], v[114:117], v[58:61], v[66:69]
	v_mfma_f32_16x16x32_f16 v[74:77], v[118:121], v[58:61], v[74:77]
	v_mfma_f32_16x16x32_f16 v[82:85], v[122:125], v[58:61], v[82:85]
	v_mfma_f32_16x16x32_f16 v[90:93], v[126:129], v[58:61], v[90:93]
	v_mfma_f32_16x16x32_f16 v[98:101], v[130:133], v[58:61], v[98:101]
	v_mfma_f32_16x16x32_f16 v[34:37], v[134:137], v[58:61], v[34:37]
	v_mfma_f32_16x16x32_f16 v[58:61], v[114:117], v[102:105], v[86:89]
	v_mfma_f32_16x16x32_f16 v[86:89], v[118:121], v[102:105], v[94:97]
	v_mfma_f32_16x16x32_f16 v[78:81], v[122:125], v[102:105], v[78:81]
	v_mfma_f32_16x16x32_f16 v[70:73], v[126:129], v[102:105], v[70:73]
	v_mfma_f32_16x16x32_f16 v[62:65], v[130:133], v[102:105], v[62:65]
	v_mfma_f32_16x16x32_f16 v[50:53], v[134:137], v[102:105], v[50:53]
	v_mfma_f32_16x16x32_f16 v[54:57], v[114:117], v[106:109], v[54:57]
	v_mfma_f32_16x16x32_f16 v[46:49], v[118:121], v[106:109], v[46:49]
	v_mfma_f32_16x16x32_f16 v[42:45], v[122:125], v[106:109], v[42:45]
	v_mfma_f32_16x16x32_f16 v[38:41], v[126:129], v[106:109], v[38:41]
	v_mfma_f32_16x16x32_f16 v[30:33], v[130:133], v[106:109], v[30:33]
	v_mfma_f32_16x16x32_f16 v[26:29], v[134:137], v[106:109], v[26:29]
	v_mfma_f32_16x16x32_f16 v[22:25], v[114:117], v[110:113], v[22:25]
	v_mfma_f32_16x16x32_f16 v[18:21], v[118:121], v[110:113], v[18:21]
	v_mfma_f32_16x16x32_f16 v[12:15], v[122:125], v[110:113], v[14:17]
	v_mfma_f32_16x16x32_f16 v[8:11], v[126:129], v[110:113], v[8:11]
	v_mfma_f32_16x16x32_f16 v[4:7], v[130:133], v[110:113], v[4:7]
	v_mfma_f32_16x16x32_f16 v[0:3], v[134:137], v[110:113], v[0:3]
	s_movk_i32 s0, 0x3400
	v_mad_u32_u24 v94, v144, s0, 0
	v_lshlrev_b32_e32 v16, 3, v145
	v_mul_u32_u24_e32 v17, 0xd0, v143
	v_add3_u32 v95, v94, v16, v17
	v_cvt_pk_f16_f32 v17, v68, v69
	v_cvt_pk_f16_f32 v16, v66, v67
	v_cvt_pk_f16_f32 v67, v76, v77
	v_cvt_pk_f16_f32 v66, v74, v75
	s_barrier
	ds_write2_b64 v95, v[16:17], v[66:67] offset1:4
	v_cvt_pk_f16_f32 v17, v84, v85
	v_cvt_pk_f16_f32 v16, v82, v83
	v_cvt_pk_f16_f32 v67, v92, v93
	v_cvt_pk_f16_f32 v66, v90, v91
	s_mov_b32 s0, 0x15555556
	ds_write2_b64 v95, v[16:17], v[66:67] offset0:8 offset1:12
	v_cvt_pk_f16_f32 v17, v100, v101
	v_cvt_pk_f16_f32 v16, v98, v99
	v_cvt_pk_f16_f32 v37, v36, v37
	v_cvt_pk_f16_f32 v36, v34, v35
	v_cvt_pk_f16_f32 v7, v6, v7
	v_cvt_pk_f16_f32 v6, v4, v5
	v_mul_hi_u32 v4, v140, s0
	ds_write2_b64 v95, v[16:17], v[36:37] offset0:16 offset1:20
	v_cvt_pk_f16_f32 v17, v60, v61
	v_cvt_pk_f16_f32 v16, v58, v59
	v_cvt_pk_f16_f32 v35, v88, v89
	v_cvt_pk_f16_f32 v34, v86, v87
	v_add_u32_e32 v36, 0x800, v95
	v_cvt_pk_f16_f32 v21, v20, v21
	v_cvt_pk_f16_f32 v20, v18, v19
	v_add_u32_e32 v18, 0x2000, v95
	v_cvt_pk_f16_f32 v15, v14, v15
	v_cvt_pk_f16_f32 v14, v12, v13
	v_cvt_pk_f16_f32 v11, v10, v11
	v_cvt_pk_f16_f32 v10, v8, v9
	v_cvt_pk_f16_f32 v3, v2, v3
	v_cvt_pk_f16_f32 v2, v0, v1
	v_mul_u32_u24_e32 v0, 12, v4
	ds_write2_b64 v36, v[16:17], v[34:35] offset0:160 offset1:164
	v_cvt_pk_f16_f32 v17, v80, v81
	v_cvt_pk_f16_f32 v16, v78, v79
	v_cvt_pk_f16_f32 v35, v72, v73
	v_cvt_pk_f16_f32 v34, v70, v71
	ds_write2_b64 v18, v[14:15], v[10:11] offset0:232 offset1:236
	v_add_u32_e32 v10, s13, v142
	v_sub_u32_e32 v5, v140, v0
	ds_write2_b64 v36, v[16:17], v[34:35] offset0:168 offset1:172
	v_cvt_pk_f16_f32 v17, v64, v65
	v_cvt_pk_f16_f32 v16, v62, v63
	v_cvt_pk_f16_f32 v35, v52, v53
	v_cvt_pk_f16_f32 v34, v50, v51
	v_lshl_add_u32 v12, v5, 3, v10
	ds_write2_b64 v36, v[16:17], v[34:35] offset0:176 offset1:180
	v_cvt_pk_f16_f32 v17, v56, v57
	v_cvt_pk_f16_f32 v16, v54, v55
	v_cvt_pk_f16_f32 v35, v48, v49
	v_cvt_pk_f16_f32 v34, v46, v47
	v_add_u32_e32 v36, 0x1800, v95
	v_lshrrev_b32_e32 v0, 10, v12
	v_mov_b32_e32 v1, 0
	ds_write2_b64 v36, v[16:17], v[34:35] offset0:64 offset1:68
	v_cvt_pk_f16_f32 v17, v44, v45
	v_cvt_pk_f16_f32 v16, v42, v43
	v_cvt_pk_f16_f32 v35, v40, v41
	v_cvt_pk_f16_f32 v34, v38, v39
	ds_write2_b64 v18, v[6:7], v[2:3] offset0:240 offset1:244
	v_add_u32_e32 v11, s12, v141
	v_lshlrev_b64 v[2:3], 23, v[0:1]
	ds_write2_b64 v36, v[16:17], v[34:35] offset0:72 offset1:76
	v_cvt_pk_f16_f32 v17, v32, v33
	v_cvt_pk_f16_f32 v16, v30, v31
	v_cvt_pk_f16_f32 v29, v28, v29
	v_cvt_pk_f16_f32 v28, v26, v27
	v_lshl_add_u64 v[6:7], s[8:9], 0, v[2:3]
	v_or_b32_e32 v2, v11, v4
	ds_write2_b64 v36, v[16:17], v[28:29] offset0:80 offset1:84
	v_cvt_pk_f16_f32 v17, v24, v25
	v_cvt_pk_f16_f32 v16, v22, v23
	v_ashrrev_i32_e32 v3, 31, v2
	ds_write2_b64 v18, v[16:17], v[20:21] offset0:224 offset1:228
	v_lshlrev_b64 v[8:9], 11, v[2:3]
	v_mul_u32_u24_e32 v0, 0xd0, v4
	v_lshlrev_b32_e32 v2, 4, v5
	s_waitcnt lgkmcnt(0)
	v_add3_u32 v0, v94, v0, v2
	ds_read_b128 v[2:5], v0
	v_and_b32_e32 v0, 0x3f8, v12
	v_lshl_add_u64 v[6:7], v[6:7], 0, v[8:9]
	v_lshlrev_b32_e32 v0, 1, v0
	v_lshl_add_u64 v[6:7], v[6:7], 0, v[0:1]
	v_or_b32_e32 v0, 64, v140
	s_waitcnt lgkmcnt(0)
	global_store_dwordx4 v[6:7], v[2:5], off sc1
	s_nop 1
	v_mul_hi_u32 v4, v0, s0
	v_mul_u32_u24_e32 v2, 12, v4
	v_sub_u32_e32 v5, v0, v2
	v_lshl_add_u32 v12, v5, 3, v10
	v_lshrrev_b32_e32 v0, 10, v12
	v_lshlrev_b64 v[2:3], 23, v[0:1]
	v_lshl_add_u64 v[6:7], s[8:9], 0, v[2:3]
	v_or_b32_e32 v2, v11, v4
	v_ashrrev_i32_e32 v3, 31, v2
	v_lshlrev_b64 v[8:9], 11, v[2:3]
	v_mul_u32_u24_e32 v0, 0xd0, v4
	v_lshlrev_b32_e32 v2, 4, v5
	v_add3_u32 v0, v94, v0, v2
	ds_read_b128 v[2:5], v0
	v_and_b32_e32 v0, 0x3f8, v12
	v_lshl_add_u64 v[6:7], v[6:7], 0, v[8:9]
	v_lshlrev_b32_e32 v0, 1, v0
	v_lshl_add_u64 v[6:7], v[6:7], 0, v[0:1]
	v_or_b32_e32 v0, 0x80, v140
	s_waitcnt lgkmcnt(0)
	global_store_dwordx4 v[6:7], v[2:5], off sc1
	s_nop 1
	v_mul_hi_u32 v4, v0, s0
	v_mul_u32_u24_e32 v2, 12, v4
	v_sub_u32_e32 v5, v0, v2
	v_lshl_add_u32 v12, v5, 3, v10
	v_lshrrev_b32_e32 v0, 10, v12
	v_lshlrev_b64 v[2:3], 23, v[0:1]
	v_lshl_add_u64 v[6:7], s[8:9], 0, v[2:3]
	v_or_b32_e32 v2, v11, v4
	v_ashrrev_i32_e32 v3, 31, v2
	v_lshlrev_b64 v[8:9], 11, v[2:3]
	v_mul_u32_u24_e32 v0, 0xd0, v4
	v_lshlrev_b32_e32 v2, 4, v5
	v_add3_u32 v0, v94, v0, v2
	ds_read_b128 v[2:5], v0
	v_and_b32_e32 v0, 0x3f8, v12
	v_lshl_add_u64 v[6:7], v[6:7], 0, v[8:9]
	v_lshlrev_b32_e32 v0, 1, v0
	v_lshl_add_u64 v[6:7], v[6:7], 0, v[0:1]
	v_or_b32_e32 v0, 0xc0, v140
	s_waitcnt lgkmcnt(0)
	global_store_dwordx4 v[6:7], v[2:5], off sc1
	s_nop 1
	v_mul_hi_u32 v4, v0, s0
	v_mul_u32_u24_e32 v2, 12, v4
	v_sub_u32_e32 v5, v0, v2
	v_lshl_add_u32 v12, v5, 3, v10
	v_lshrrev_b32_e32 v0, 10, v12
	v_lshlrev_b64 v[2:3], 23, v[0:1]
	v_lshl_add_u64 v[6:7], s[8:9], 0, v[2:3]
	v_or_b32_e32 v2, v11, v4
	v_ashrrev_i32_e32 v3, 31, v2
	v_lshlrev_b64 v[8:9], 11, v[2:3]
	v_mul_u32_u24_e32 v0, 0xd0, v4
	v_lshlrev_b32_e32 v2, 4, v5
	v_add3_u32 v0, v94, v0, v2
	ds_read_b128 v[2:5], v0
	v_and_b32_e32 v0, 0x3f8, v12
	v_lshl_add_u64 v[6:7], v[6:7], 0, v[8:9]
	v_lshlrev_b32_e32 v0, 1, v0
	v_lshl_add_u64 v[6:7], v[6:7], 0, v[0:1]
	v_or_b32_e32 v0, 0x100, v140
	s_waitcnt lgkmcnt(0)
	global_store_dwordx4 v[6:7], v[2:5], off sc1
	s_nop 1
	v_mul_hi_u32 v4, v0, s0
	v_mul_u32_u24_e32 v2, 12, v4
	v_sub_u32_e32 v5, v0, v2
	v_lshl_add_u32 v12, v5, 3, v10
	v_lshrrev_b32_e32 v0, 10, v12
	v_lshlrev_b64 v[2:3], 23, v[0:1]
	v_lshl_add_u64 v[6:7], s[8:9], 0, v[2:3]
	v_or_b32_e32 v2, v11, v4
	v_ashrrev_i32_e32 v3, 31, v2
	v_lshlrev_b64 v[8:9], 11, v[2:3]
	v_mul_u32_u24_e32 v0, 0xd0, v4
	v_lshlrev_b32_e32 v2, 4, v5
	v_add3_u32 v0, v94, v0, v2
	ds_read_b128 v[2:5], v0
	v_and_b32_e32 v0, 0x3f8, v12
	v_lshl_add_u64 v[6:7], v[6:7], 0, v[8:9]
	v_lshlrev_b32_e32 v0, 1, v0
	v_lshl_add_u64 v[6:7], v[6:7], 0, v[0:1]
	v_or_b32_e32 v0, 0x140, v140
	s_waitcnt lgkmcnt(0)
	global_store_dwordx4 v[6:7], v[2:5], off sc1
	s_nop 1
	v_mul_hi_u32 v4, v0, s0
	v_mul_u32_u24_e32 v2, 12, v4
	v_sub_u32_e32 v5, v0, v2
	v_lshl_add_u32 v12, v5, 3, v10
	v_lshrrev_b32_e32 v0, 10, v12
	v_lshlrev_b64 v[2:3], 23, v[0:1]
	v_lshl_add_u64 v[6:7], s[8:9], 0, v[2:3]
	v_or_b32_e32 v2, v11, v4
	v_ashrrev_i32_e32 v3, 31, v2
	v_lshlrev_b64 v[8:9], 11, v[2:3]
	v_mul_u32_u24_e32 v0, 0xd0, v4
	v_lshlrev_b32_e32 v2, 4, v5
	v_add3_u32 v0, v94, v0, v2
	ds_read_b128 v[2:5], v0
	v_and_b32_e32 v0, 0x3f8, v12
	v_lshl_add_u64 v[6:7], v[6:7], 0, v[8:9]
	v_lshlrev_b32_e32 v0, 1, v0
	v_lshl_add_u64 v[6:7], v[6:7], 0, v[0:1]
	v_or_b32_e32 v0, 0x180, v140
	s_waitcnt lgkmcnt(0)
	global_store_dwordx4 v[6:7], v[2:5], off sc1
	s_nop 1
	v_mul_hi_u32 v4, v0, s0
	v_mul_u32_u24_e32 v2, 12, v4
	v_sub_u32_e32 v5, v0, v2
	v_lshl_add_u32 v12, v5, 3, v10
	v_lshrrev_b32_e32 v0, 10, v12
	v_lshlrev_b64 v[2:3], 23, v[0:1]
	v_lshl_add_u64 v[6:7], s[8:9], 0, v[2:3]
	v_or_b32_e32 v2, v11, v4
	v_ashrrev_i32_e32 v3, 31, v2
	v_lshlrev_b64 v[8:9], 11, v[2:3]
	v_mul_u32_u24_e32 v0, 0xd0, v4
	v_lshlrev_b32_e32 v2, 4, v5
	v_add3_u32 v0, v94, v0, v2
	ds_read_b128 v[2:5], v0
	v_and_b32_e32 v0, 0x3f8, v12
	v_lshl_add_u64 v[6:7], v[6:7], 0, v[8:9]
	v_lshlrev_b32_e32 v0, 1, v0
	v_lshl_add_u64 v[6:7], v[6:7], 0, v[0:1]
	v_or_b32_e32 v0, 0x1c0, v140
	s_waitcnt lgkmcnt(0)
	global_store_dwordx4 v[6:7], v[2:5], off sc1
	s_nop 1
	v_mul_hi_u32 v4, v0, s0
	v_mul_u32_u24_e32 v2, 12, v4
	v_sub_u32_e32 v5, v0, v2
	v_lshl_add_u32 v12, v5, 3, v10
	v_lshrrev_b32_e32 v0, 10, v12
	v_lshlrev_b64 v[2:3], 23, v[0:1]
	v_lshl_add_u64 v[6:7], s[8:9], 0, v[2:3]
	v_or_b32_e32 v2, v11, v4
	v_ashrrev_i32_e32 v3, 31, v2
	v_lshlrev_b64 v[8:9], 11, v[2:3]
	v_mul_u32_u24_e32 v0, 0xd0, v4
	v_lshlrev_b32_e32 v2, 4, v5
	v_add3_u32 v0, v94, v0, v2
	ds_read_b128 v[2:5], v0
	v_and_b32_e32 v0, 0x3f8, v12
	v_lshl_add_u64 v[6:7], v[6:7], 0, v[8:9]
	v_lshlrev_b32_e32 v0, 1, v0
	v_lshl_add_u64 v[6:7], v[6:7], 0, v[0:1]
	v_or_b32_e32 v0, 0x200, v140
	s_waitcnt lgkmcnt(0)
	global_store_dwordx4 v[6:7], v[2:5], off sc1
	s_nop 1
	v_mul_hi_u32 v4, v0, s0
	v_mul_u32_u24_e32 v2, 12, v4
	v_sub_u32_e32 v5, v0, v2
	v_lshl_add_u32 v12, v5, 3, v10
	v_lshrrev_b32_e32 v0, 10, v12
	v_lshlrev_b64 v[2:3], 23, v[0:1]
	v_lshl_add_u64 v[6:7], s[8:9], 0, v[2:3]
	v_or_b32_e32 v2, v11, v4
	v_ashrrev_i32_e32 v3, 31, v2
	v_lshlrev_b64 v[8:9], 11, v[2:3]
	v_mul_u32_u24_e32 v0, 0xd0, v4
	v_lshlrev_b32_e32 v2, 4, v5
	v_add3_u32 v0, v94, v0, v2
	ds_read_b128 v[2:5], v0
	v_and_b32_e32 v0, 0x3f8, v12
	v_lshl_add_u64 v[6:7], v[6:7], 0, v[8:9]
	v_lshlrev_b32_e32 v0, 1, v0
	v_lshl_add_u64 v[6:7], v[6:7], 0, v[0:1]
	v_or_b32_e32 v0, 0x240, v140
	s_waitcnt lgkmcnt(0)
	global_store_dwordx4 v[6:7], v[2:5], off sc1
	s_nop 1
	v_mul_hi_u32 v4, v0, s0
	v_mul_u32_u24_e32 v2, 12, v4
	v_sub_u32_e32 v5, v0, v2
	v_lshl_add_u32 v12, v5, 3, v10
	v_lshrrev_b32_e32 v0, 10, v12
	v_lshlrev_b64 v[2:3], 23, v[0:1]
	v_lshl_add_u64 v[6:7], s[8:9], 0, v[2:3]
	v_or_b32_e32 v2, v11, v4
	v_ashrrev_i32_e32 v3, 31, v2
	v_lshlrev_b64 v[8:9], 11, v[2:3]
	v_mul_u32_u24_e32 v0, 0xd0, v4
	v_lshlrev_b32_e32 v2, 4, v5
	v_add3_u32 v0, v94, v0, v2
	ds_read_b128 v[2:5], v0
	v_and_b32_e32 v0, 0x3f8, v12
	v_lshl_add_u64 v[6:7], v[6:7], 0, v[8:9]
	v_lshlrev_b32_e32 v0, 1, v0
	v_lshl_add_u64 v[6:7], v[6:7], 0, v[0:1]
	v_or_b32_e32 v0, 0x280, v140
	s_waitcnt lgkmcnt(0)
	global_store_dwordx4 v[6:7], v[2:5], off sc1
	s_nop 1
	v_mul_hi_u32 v4, v0, s0
	v_mul_u32_u24_e32 v2, 12, v4
	v_sub_u32_e32 v5, v0, v2
	v_lshl_add_u32 v12, v5, 3, v10
	v_lshrrev_b32_e32 v0, 10, v12
	v_lshlrev_b64 v[2:3], 23, v[0:1]
	v_lshl_add_u64 v[6:7], s[8:9], 0, v[2:3]
	v_or_b32_e32 v2, v11, v4
	v_ashrrev_i32_e32 v3, 31, v2
	v_lshlrev_b64 v[8:9], 11, v[2:3]
	v_mul_u32_u24_e32 v0, 0xd0, v4
	v_lshlrev_b32_e32 v2, 4, v5
	v_add3_u32 v0, v94, v0, v2
	ds_read_b128 v[2:5], v0
	v_and_b32_e32 v0, 0x3f8, v12
	v_lshl_add_u64 v[6:7], v[6:7], 0, v[8:9]
	v_lshlrev_b32_e32 v0, 1, v0
	v_lshl_add_u64 v[6:7], v[6:7], 0, v[0:1]
	v_or_b32_e32 v0, 0x2c0, v140
	s_waitcnt lgkmcnt(0)
	global_store_dwordx4 v[6:7], v[2:5], off sc1
	s_nop 1
	v_mul_hi_u32 v4, v0, s0
	v_mul_u32_u24_e32 v2, 12, v4
	v_sub_u32_e32 v5, v0, v2
	v_lshl_add_u32 v10, v5, 3, v10
	v_lshrrev_b32_e32 v0, 10, v10
	v_lshlrev_b64 v[2:3], 23, v[0:1]
	v_lshl_add_u64 v[6:7], s[8:9], 0, v[2:3]
	v_or_b32_e32 v2, v11, v4
	v_ashrrev_i32_e32 v3, 31, v2
	v_lshlrev_b64 v[8:9], 11, v[2:3]
	v_mul_u32_u24_e32 v0, 0xd0, v4
	v_lshlrev_b32_e32 v2, 4, v5
	v_add3_u32 v0, v94, v0, v2
	ds_read_b128 v[2:5], v0
	v_and_b32_e32 v0, 0x3f8, v10
	v_lshl_add_u64 v[6:7], v[6:7], 0, v[8:9]
	v_lshlrev_b32_e32 v0, 1, v0
	v_lshl_add_u64 v[0:1], v[6:7], 0, v[0:1]
	s_waitcnt lgkmcnt(0)
	global_store_dwordx4 v[0:1], v[2:5], off sc1
	s_nop 1
	s_endpgm
	s_nop 0
	s_nop 0
	s_nop 0
	s_nop 0
	s_nop 0
	s_nop 0
	s_nop 0
	s_nop 0
	s_nop 0
	s_nop 0
	s_nop 0
	s_nop 0
	s_nop 0
	s_nop 0
	s_nop 0
	s_nop 0
	s_nop 0
	s_endpgm

	.amdhsa_kernel _Z8gemm16_kILi256ELi192ELi0ELi2EEvPKDF16_S1_PvPKfi
		.amdhsa_group_segment_fixed_size 0
		.amdhsa_private_segment_fixed_size 0
		.amdhsa_kernarg_size 36
		.amdhsa_user_sgpr_count 2
		.amdhsa_user_sgpr_dispatch_ptr 0
		.amdhsa_user_sgpr_queue_ptr 0
		.amdhsa_user_sgpr_kernarg_segment_ptr 1
		.amdhsa_user_sgpr_dispatch_id 0
		.amdhsa_user_sgpr_kernarg_preload_length 0
		.amdhsa_user_sgpr_kernarg_preload_offset 0
		.amdhsa_user_sgpr_private_segment_size 0
		.amdhsa_uses_dynamic_stack 0
		.amdhsa_enable_private_segment 0
		.amdhsa_system_sgpr_workgroup_id_x 1
		.amdhsa_system_sgpr_workgroup_id_y 0
		.amdhsa_system_sgpr_workgroup_id_z 0
		.amdhsa_system_sgpr_workgroup_info 0
		.amdhsa_system_vgpr_workitem_id 0
		.amdhsa_next_free_vgpr 216
		.amdhsa_next_free_sgpr 26
		.amdhsa_accum_offset 216
		.amdhsa_reserve_vcc 1
		.amdhsa_float_round_mode_32 0
		.amdhsa_float_round_mode_16_64 0
		.amdhsa_float_denorm_mode_32 3
		.amdhsa_float_denorm_mode_16_64 3
		.amdhsa_dx10_clamp 1
		.amdhsa_ieee_mode 1
		.amdhsa_fp16_overflow 0
		.amdhsa_tg_split 0
		.amdhsa_exception_fp_ieee_invalid_op 0
		.amdhsa_exception_fp_denorm_src 0
		.amdhsa_exception_fp_ieee_div_zero 0
		.amdhsa_exception_fp_ieee_overflow 0
		.amdhsa_exception_fp_ieee_underflow 0
		.amdhsa_exception_fp_ieee_inexact 0
		.amdhsa_exception_int_div_zero 0
	.end_amdhsa_kernel

amdhsa.kernels:
  - .agpr_count:     0
    .args:
      - .address_space:  global
        .offset:         0
        .size:           8
        .value_kind:     global_buffer
      - .address_space:  global
        .offset:         8
        .size:           8
        .value_kind:     global_buffer
      - .address_space:  global
        .offset:         16
        .size:           8
        .value_kind:     global_buffer
      - .address_space:  global
        .offset:         24
        .size:           8
        .value_kind:     global_buffer
      - .address_space:  global
        .offset:         32
        .size:           8
        .value_kind:     global_buffer
      - .address_space:  global
        .offset:         40
        .size:           8
        .value_kind:     global_buffer
      - .address_space:  global
        .offset:         48
        .size:           8
        .value_kind:     global_buffer
      - .address_space:  global
        .offset:         56
        .size:           8
        .value_kind:     global_buffer
    .group_segment_fixed_size: 0
    .kernarg_segment_align: 8
    .kernarg_segment_size: 64
    .language:       OpenCL C
    .language_version:
      - 2
      - 0
    .max_flat_workgroup_size: 256
    .name:           _Z10cvt_kernelPKfS0_S0_S0_S0_PDF16_S1_S1_
    .private_segment_fixed_size: 0
    .sgpr_count:     20
    .sgpr_spill_count: 0
    .symbol:         _Z10cvt_kernelPKfS0_S0_S0_S0_PDF16_S1_S1_.kd
    .uniform_work_group_size: 1
    .uses_dynamic_stack: false
    .vgpr_count:     70
    .vgpr_spill_count: 0
    .wavefront_size: 64
  - .agpr_count:     0
    .args:
      - .address_space:  global
        .offset:         0
        .size:           8
        .value_kind:     global_buffer
      - .address_space:  global
        .offset:         8
        .size:           8
        .value_kind:     global_buffer
      - .address_space:  global
        .offset:         16
        .size:           8
        .value_kind:     global_buffer
      - .address_space:  global
        .offset:         24
        .size:           8
        .value_kind:     global_buffer
    .group_segment_fixed_size: 0
    .kernarg_segment_align: 8
    .kernarg_segment_size: 32
    .language:       OpenCL C
    .language_version:
      - 2
      - 0
    .max_flat_workgroup_size: 512
    .name:           _Z10attn64_fwdPKDF16_S0_S0_PDF16_
    .private_segment_fixed_size: 0
    .sgpr_count:     57
    .sgpr_spill_count: 0
    .symbol:         _Z10attn64_fwdPKDF16_S0_S0_PDF16_.kd
    .uniform_work_group_size: 1
    .uses_dynamic_stack: false
    .vgpr_count:     219
    .vgpr_spill_count: 0
    .wavefront_size: 64
  - .agpr_count:     0
    .args:
      - .address_space:  global
        .offset:         0
        .size:           8
        .value_kind:     global_buffer
      - .address_space:  global
        .offset:         8
        .size:           8
        .value_kind:     global_buffer
      - .address_space:  global
        .offset:         16
        .size:           8
        .value_kind:     global_buffer
      - .actual_access:  read_only
        .address_space:  global
        .offset:         24
        .size:           8
        .value_kind:     global_buffer
      - .offset:         32
        .size:           4
        .value_kind:     by_value
    .group_segment_fixed_size: 0
    .kernarg_segment_align: 8
    .kernarg_segment_size: 36
    .language:       OpenCL C
    .language_version:
      - 2
      - 0
    .max_flat_workgroup_size: 512
    .name:           _Z8gemm16_kILi256ELi192ELi0ELi2EEvPKDF16_S1_PvPKfi
    .private_segment_fixed_size: 0
    .sgpr_count:     32
    .sgpr_spill_count: 0
    .symbol:         _Z8gemm16_kILi256ELi192ELi0ELi2EEvPKDF16_S1_PvPKfi.kd
    .uniform_work_group_size: 1
    .uses_dynamic_stack: false
    .vgpr_count:     216
    .vgpr_spill_count: 0
    .wavefront_size: 64
  - .agpr_count:     0
    .args:
      - .address_space:  global
        .offset:         0
        .size:           8
        .value_kind:     global_buffer
      - .address_space:  global
        .offset:         8
        .size:           8
        .value_kind:     global_buffer
      - .address_space:  global
        .offset:         16
        .size:           8
        .value_kind:     global_buffer
      - .actual_access:  read_only
        .address_space:  global
        .offset:         24
        .size:           8
        .value_kind:     global_buffer
      - .offset:         32
        .size:           4
        .value_kind:     by_value
    .group_segment_fixed_size: 0
    .kernarg_segment_align: 8
    .kernarg_segment_size: 36
    .language:       OpenCL C
    .language_version:
      - 2
      - 0
    .max_flat_workgroup_size: 512
    .name:           _Z8gemm16_kILi128ELi128ELi1ELi3EEvPKDF16_S1_PvPKfi
    .private_segment_fixed_size: 0
    .sgpr_count:     28
    .sgpr_spill_count: 0
    .symbol:         _Z8gemm16_kILi128ELi128ELi1ELi3EEvPKDF16_S1_PvPKfi.kd
    .uniform_work_group_size: 1
    .uses_dynamic_stack: false
    .vgpr_count:     104
    .vgpr_spill_count: 0
    .wavefront_size: 64
